# fp8 conversion of w_in, w_out and shared expert weights folded into the hand-written 128x64 tile loop (compiled segments skipped)
# baseline (speedup 1.0000x reference)
.LBB0_5:
	s_or_b64 exec, exec, s[4:5]
	v_readlane_b32 s8, v255, 0
	v_readlane_b32 s9, v255, 1
	s_load_dwordx2 s[2:3], s[8:9], 0xe0
	v_mov_b32_e32 v0, 0
	s_lshr_b32 s1, s10, 6
	s_waitcnt lgkmcnt(0)
	s_mul_i32 s0, s1, 0x2100
	v_mbcnt_lo_u32_b32 v0, -1, v0
	v_mbcnt_hi_u32_b32 v0, -1, v0
	s_add_i32 s38, s0, 0
	s_mov_b32 s4, s96
	v_add_u32_e32 v0, s97, v0
	s_mov_b32 s5, s33
	s_add_u32 s39, s2, 0x600200
	s_addc_u32 s40, s3, 0
	s_lshl_b32 s41, s5, 3
	s_abs_i32 s42, s41
	v_cvt_f32_u32_e32 v0, s42
	s_load_dwordx2 s[10:11], s[8:9], 0x28
	s_lshl_b32 s43, s4, 3
	s_add_i32 s43, s43, s1
	v_rcp_iflag_f32_e32 v0, v0
	s_sub_i32 s1, 0, s42
	s_mov_b32 s0, 0
	v_mov_b32_e32 v65, 0
	v_mul_f32_e32 v0, 0x4f7ffffe, v0
	v_cvt_u32_f32_e32 v0, v0
	s_lshl_b32 s45, s5, 7
	s_mov_b64 s[14:15], 0
	s_mov_b64 s[12:13], -1
	v_readfirstlane_b32 s2, v0
	s_mul_i32 s1, s1, s2
	s_mul_hi_u32 s1, s2, s1
	s_add_i32 s44, s2, s1
	s_movk_i32 s46, 0xfd0
	s_movk_i32 s47, 0x3f40
	s_movk_i32 s48, 0x44
	s_movk_i32 s49, 0x800
	s_movk_i32 s50, 0x1200
	s_movk_i32 s51, 0x480
	s_movk_i32 s52, 0x84
	s_movk_i32 s53, 0x300
	s_movk_i32 s54, 0x1800
	s_movk_i32 s55, 0x600
	s_movk_i32 s56, 0x200
	s_movk_i32 s57, 0x80
	v_mov_b32_e32 v68, 0x42000000
	s_branch .LBB0_8
.LBB0_7:
	s_add_i32 s1, s0, 0x100
	s_sub_i32 s0, 0xffffff00, s0
	s_max_i32 s0, s1, s0
	s_ashr_i32 s4, s1, 31
	s_mul_hi_u32 s1, s0, s44
	s_mul_i32 s1, s1, s42
	s_sub_i32 s0, s0, s1
	s_xor_b64 s[2:3], s[12:13], -1
	s_sub_i32 s1, s0, s42
	s_cmp_ge_u32 s0, s42
	s_cselect_b32 s0, s1, s0
	s_sub_i32 s1, s0, s42
	s_cmp_ge_u32 s0, s42
	s_cselect_b32 s0, s1, s0
	s_xor_b32 s0, s0, s4
	s_sub_i32 s0, s0, s4
	s_mov_b64 s[14:15], 1
	s_mov_b64 s[12:13], 0
	s_and_b64 vcc, exec, s[2:3]
	s_cbranch_vccnz .LBB0_117
.LBB0_8:
	s_mul_i32 s1, s14, 0x19fb0000
	s_add_u32 s18, s39, s1
	s_addc_u32 s19, s40, 0
	s_sub_i32 s1, s43, s0
	s_ashr_i32 s16, s1, 31
	s_abs_i32 s1, s1
	s_mul_hi_u32 s17, s1, s44
	s_mul_i32 s17, s17, s42
	s_sub_i32 s1, s1, s17
	s_waitcnt lgkmcnt(0)
	s_mov_b64 s[2:3], s[10:11]
	s_sub_i32 s17, s1, s42
	s_load_dwordx4 s[4:7], s[8:9], 0x50
	s_load_dwordx2 s[36:37], s[8:9], 0x80
	s_cmp_ge_u32 s1, s42
	s_cselect_b32 s1, s17, s1
	s_sub_i32 s17, s1, s42
	s_cmp_ge_u32 s1, s42
	s_cselect_b32 s1, s17, s1
	s_waitcnt lgkmcnt(0)
	s_load_dwordx2 s[34:35], s[8:9], 0xa8
	s_xor_b32 s1, s1, s16
	s_waitcnt lgkmcnt(0)
	s_load_dwordx2 s[30:31], s[8:9], 0xb0
	s_sub_i32 s1, s1, s16
	s_waitcnt lgkmcnt(0)
	s_load_dwordx2 s[26:27], s[8:9], 0xb8
	s_ashr_i32 s16, s1, 31
	s_waitcnt lgkmcnt(0)
	s_load_dwordx2 s[24:25], s[8:9], 0xc0
	s_and_b32 s59, s16, s41
	s_waitcnt lgkmcnt(0)
	s_load_dwordx2 s[22:23], s[8:9], 0xc8
	s_add_i32 s59, s59, s1
	s_waitcnt lgkmcnt(0)
	s_load_dwordx2 s[20:21], s[8:9], 0xd0
	s_cmpk_gt_i32 s59, 0x7ff
	s_waitcnt lgkmcnt(0)
	s_branch .LBB0_13

.LBB0_83:
	s_add_i32 s1, s0, 0x60
	s_sub_i32 s0, 0xffffffa0, s0
	s_max_i32 s0, s1, s0
	s_ashr_i32 s2, s1, 31
	s_mul_hi_u32 s1, s0, s44
	s_mul_i32 s1, s1, s42
	s_sub_i32 s0, s0, s1
	s_sub_i32 s1, s0, s42
	s_cmp_ge_u32 s0, s42
	s_cselect_b32 s0, s1, s0
	s_sub_i32 s1, s0, s42
	s_cmp_ge_u32 s0, s42
	s_cselect_b32 s0, s1, s0
	s_xor_b32 s0, s0, s2
	s_sub_i32 s16, s0, s2
	s_sub_i32 s0, s43, s16
	s_ashr_i32 s1, s0, 31
	s_abs_i32 s0, s0
	s_mul_hi_u32 s2, s0, s44
	s_mul_i32 s2, s2, s42
	s_sub_i32 s0, s0, s2
	s_sub_i32 s2, s0, s42
	s_cmp_ge_u32 s0, s42
	s_cselect_b32 s0, s2, s0
	s_sub_i32 s2, s0, s42
	s_cmp_ge_u32 s0, s42
	s_cselect_b32 s0, s2, s0
	s_xor_b32 s0, s0, s1
	s_sub_i32 s0, s0, s1
	s_ashr_i32 s1, s0, 31
	s_and_b32 s29, s1, s41
	s_add_i32 s29, s29, s0
	s_cmpk_gt_i32 s29, 0x3ff
	s_branch .LBB0_88

.LBB0_103:
	s_add_i32 s1, s0, 0x4000
	s_sub_i32 s0, 0xffffc000, s0
	s_max_i32 s0, s1, s0
	s_ashr_i32 s2, s1, 31
	s_mul_hi_u32 s1, s0, s44
	s_mul_i32 s1, s1, s42
	s_sub_i32 s0, s0, s1
	s_lshl_b64 s[6:7], s[14:15], 20
	s_sub_i32 s1, s0, s42
	s_cmp_ge_u32 s0, s42
	s_cselect_b32 s0, s1, s0
	s_sub_i32 s1, s0, s42
	s_cmp_ge_u32 s0, s42
	s_cselect_b32 s0, s1, s0
	s_xor_b32 s0, s0, s2
	s_sub_i32 s0, s0, s2
	s_add_u32 s4, s18, 0x99b0000
	s_addc_u32 s5, s19, 0
	s_sub_i32 s1, s43, s0
	s_ashr_i32 s2, s1, 31
	s_abs_i32 s1, s1
	s_mul_hi_u32 s3, s1, s44
	s_mul_i32 s3, s3, s42
	s_sub_i32 s1, s1, s3
	s_sub_i32 s3, s1, s42
	s_cmp_ge_u32 s1, s42
	s_cselect_b32 s1, s3, s1
	s_sub_i32 s3, s1, s42
	s_cmp_ge_u32 s1, s42
	s_cselect_b32 s1, s3, s1
	s_xor_b32 s1, s1, s2
	s_sub_i32 s1, s1, s2
	s_ashr_i32 s2, s1, 31
	s_and_b32 s27, s2, s41
	s_add_i32 s27, s27, s1
	s_cmpk_gt_i32 s27, 0xff
	s_branch .LBB0_108
.LBB0_108:
	s_add_i32 s1, s0, 0x100
	s_sub_i32 s0, 0xffffff00, s0
	s_max_i32 s0, s1, s0
	s_ashr_i32 s2, s1, 31
	s_mul_hi_u32 s1, s0, s44
	s_mul_i32 s1, s1, s42
	s_sub_i32 s0, s0, s1
	s_sub_i32 s1, s0, s42
	s_cmp_ge_u32 s0, s42
	s_cselect_b32 s0, s1, s0
	s_sub_i32 s1, s0, s42
	s_cmp_ge_u32 s0, s42
	s_cselect_b32 s0, s1, s0
	s_xor_b32 s0, s0, s2
	s_sub_i32 s0, s0, s2
	s_sub_i32 s1, s43, s0
	s_ashr_i32 s2, s1, 31
	s_abs_i32 s1, s1
	s_mul_hi_u32 s3, s1, s44
	s_mul_i32 s3, s3, s42
	s_sub_i32 s1, s1, s3
	s_sub_i32 s3, s1, s42
	s_cmp_ge_u32 s1, s42
	s_cselect_b32 s1, s3, s1
	s_sub_i32 s3, s1, s42
	s_cmp_ge_u32 s1, s42
	s_cselect_b32 s1, s3, s1
	s_xor_b32 s1, s1, s2
	s_sub_i32 s1, s1, s2
	s_ashr_i32 s2, s1, 31
	s_and_b32 s24, s2, s41
	s_add_i32 s24, s24, s1
	s_cmpk_gt_i32 s24, 0xff
	s_branch .LBB0_113
.LBB0_113:
	s_add_i32 s1, s0, 0x100
	s_sub_i32 s0, 0xffffff00, s0
	s_max_i32 s0, s1, s0
	s_ashr_i32 s2, s1, 31
	s_mul_hi_u32 s1, s0, s44
	s_mul_i32 s1, s1, s42
	s_sub_i32 s0, s0, s1
	s_sub_i32 s1, s0, s42
	s_cmp_ge_u32 s0, s42
	s_cselect_b32 s0, s1, s0
	s_sub_i32 s1, s0, s42
	s_cmp_ge_u32 s0, s42
	s_cselect_b32 s0, s1, s0
	s_xor_b32 s0, s0, s2
	s_sub_i32 s0, s0, s2
	s_sub_i32 s1, s43, s0
	s_ashr_i32 s2, s1, 31
	s_abs_i32 s1, s1
	s_mul_hi_u32 s3, s1, s44
	s_mul_i32 s3, s3, s42
	s_sub_i32 s1, s1, s3
	s_sub_i32 s3, s1, s42
	s_cmp_ge_u32 s1, s42
	s_cselect_b32 s1, s3, s1
	s_sub_i32 s3, s1, s42
	s_cmp_ge_u32 s1, s42
	s_cselect_b32 s1, s3, s1
	s_xor_b32 s1, s1, s2
	s_sub_i32 s1, s1, s2
	s_ashr_i32 s2, s1, 31
	s_and_b32 s17, s2, s41
	s_add_i32 s17, s17, s1
	s_cmpk_gt_i32 s17, 0xff
	s_branch .LBB0_7
.LBB0_117:
	v_readlane_b32 s0, v255, 0
	v_readlane_b32 s1, v255, 1
	s_nop 4
	s_load_dwordx2 s[2:3], s[0:1], 0xa8
	s_load_dwordx2 s[4:5], s[0:1], 0xb0
	s_load_dwordx2 s[6:7], s[0:1], 0xb8
	s_load_dwordx2 s[8:9], s[0:1], 0xe0
	s_load_dwordx2 s[70:71], s[0:1], 0x28
	s_load_dwordx2 s[72:73], s[0:1], 0x80
	s_load_dwordx2 s[74:75], s[0:1], 0xc0
	s_load_dwordx2 s[76:77], s[0:1], 0xc8
	s_load_dwordx2 s[78:79], s[0:1], 0xd0
	s_load_dword s11, s[0:1], 0xf0
	v_mbcnt_lo_u32_b32 v212, -1, 0
	v_mbcnt_hi_u32_b32 v212, -1, v212
	v_lshrrev_b32_e32 v174, 4, v212
	v_and_b32_e32 v175, 15, v212
	v_lshlrev_b32_e32 v175, 4, v175
	v_lshrrev_b32_e32 v176, 3, v212
	v_and_b32_e32 v177, 7, v212
	v_lshlrev_b32_e32 v177, 4, v177
	v_mov_b32_e32 v178, 0x42000000
	v_mov_b32_e32 v179, 0x42000000
	v_mov_b32_e32 v217, 0x42000000
	v_mov_b32_e32 v218, v175
	v_cmp_gt_u32_e32 vcc, 64, v175
	s_nop 1
	v_cndmask_b32_e32 v217, 0, v217, vcc
	v_cndmask_b32_e32 v218, 0, v218, vcc
	s_lshr_b32 s56, s97, 6
	s_mul_i32 s29, s56, 0x2100
	s_lshl_b32 s10, s96, 3
	s_add_u32 s10, s10, s56
	v_mul_u32_u24_e32 v172, 33, v175
	v_lshl_add_u32 v172, v174, 2, v172
	v_add_u32_e32 v172, s29, v172
	v_mul_u32_u24_e32 v173, 0x84, v176
	v_add3_u32 v173, v173, v177, s29
	s_waitcnt lgkmcnt(0)
	s_add_u32 s8, s8, 0x600200
	s_addc_u32 s9, s9, 0
	s_lshl_b32 s11, s11, 3
	s_mov_b32 s13, s10
	s_cmp_lt_u32 s13, 0xcf00
	s_cbranch_scc0 .Lxc_done
	s_mov_b32 s81, 0
	s_mov_b32 s80, 0
	s_cmp_lt_u32 s13, 0xc000
	s_cbranch_scc0 .Lxp_other0
	s_lshr_b32 s56, s13, 13
	s_and_b32 s57, s13, 0x1fff
	s_mov_b32 s85, 0
	s_branch .Lxp_exp0
.Lxp_other0:
	s_sub_u32 s56, s13, 0xc000
	s_cmp_lt_u32 s56, 0xc00
	s_cbranch_scc1 .Lxp_dense0
	s_sub_u32 s57, s56, 0xc00
	s_lshr_b32 s56, s57, 7
	s_and_b32 s57, s57, 0x7f
	s_mov_b32 s85, 1
.Lxp_exp0:
	s_cmp_ge_u32 s56, 3
	s_cselect_b32 s58, 1, 0
	s_mul_i32 s59, s58, 3
	s_sub_u32 s59, s56, s59
	s_lshr_b32 s64, s57, 7
	s_and_b32 s65, s57, 0x7f
	s_cmp_eq_u32 s59, 2
	s_cselect_b32 s56, 2, 0
	s_cselect_b32 s66, 2, 4
	s_lshl_b32 s26, 0x800, s56
	s_lshr_b32 s63, 0x800, s56
	s_lshr_b32 s67, s65, s66
	s_lshl_b32 s56, s67, s66
	s_sub_u32 s65, s65, s56
	s_cmp_eq_u32 s59, 0
	s_cselect_b32 s68, s2, s4
	s_cselect_b32 s69, s3, s5
	s_cselect_b32 s86, s74, s76
	s_cselect_b32 s87, s75, s77
	s_cmp_eq_u32 s59, 2
	s_cselect_b32 s68, s6, s68
	s_cselect_b32 s69, s7, s69
	s_cselect_b32 s86, s78, s86
	s_cselect_b32 s87, s79, s87
	s_cmp_eq_u32 s85, 1
	s_cselect_b32 s68, s86, s68
	s_cselect_b32 s69, s87, s69
	s_cselect_b32 s82, 22, 28
	s_cselect_b32 s83, 0, s64
	s_cselect_b32 s84, 64, s64
	s_lshl_b32 s56, s58, s82
	s_lshl_b32 s57, s83, 22
	s_add_u32 s56, s56, s57
	s_lshl_b32 s57, s65, 7
	s_mul_i32 s57, s57, s26
	s_add_u32 s56, s56, s57
	s_lshl_b32 s57, s67, 8
	s_add_u32 s56, s56, s57
	s_mul_i32 s27, s26, 13
	s_lshl_b32 s28, s26, 2
	s_mul_i32 s86, s58, 0x19fb0000
	s_lshl_b32 s57, s65, 7
	s_add_u32 s86, s86, s57
	s_lshr_b32 s57, s67, 1
	s_lshl_b32 s57, s57, 8
	s_and_b32 s66, s67, 1
	s_lshl_b32 s66, s66, 6
	s_add_u32 s57, s57, s66
	s_lshl_b32 s66, s59, 7
	s_add_u32 s57, s57, s66
	s_lshl_b32 s57, s57, 11
	s_lshl_b32 s66, s84, 21
	s_add_u32 s57, s57, s66
	s_add_u32 s57, s57, 0x19b0000
	s_lshl_b32 s66, s67, 15
	s_lshl_b32 s87, s84, 20
	s_add_u32 s66, s66, s87
	s_add_u32 s66, s66, 0x11db0000
	s_cmp_eq_u32 s59, 2
	s_cselect_b32 s57, s66, s57
	s_add_u32 s57, s57, s86
	s_branch .Lxp_tail0
.Lxp_dense0:
	s_cmp_lt_u32 s56, 2048
	s_cbranch_scc0 .Lxp_wout0
	s_lshr_b32 s58, s56, 10
	s_and_b32 s57, s56, 0x3ff
	s_and_b32 s65, s57, 15
	s_lshr_b32 s67, s57, 4
	s_movk_i32 s87, 0x3f40
	s_mov_b64 s[68:69], s[70:71]
	s_mul_i32 s56, s58, 0x1fa0000
	s_mul_i32 s86, s58, 0x19fb0000
	s_mov_b32 s26, s87
	s_mul_i32 s27, s87, 13
	s_lshl_b32 s28, s87, 2
	s_cmp_eq_u32 s67, 63
	s_cselect_b32 s81, 1, 0
	s_branch .Lxp_dcom0
.Lxp_wout0:
	s_sub_u32 s56, s56, 2048
	s_lshr_b32 s58, s56, 9
	s_and_b32 s57, s56, 0x1ff
	s_and_b32 s65, s57, 15
	s_lshr_b32 s67, s57, 4
	s_movk_i32 s87, 0x2000
	s_mov_b64 s[68:69], s[72:73]
	s_lshl_b32 s56, s58, 24
	s_mul_i32 s86, s58, 0x19fb0000
	s_add_u32 s86, s86, 0x11b0000
	s_cmp_lt_u32 s65, 12
	s_cbranch_scc0 .Lxp_wnp0
	s_mov_b32 s26, 0x40000
	s_mov_b32 s27, 0xfff48000
	s_mov_b32 s80, -1
	s_movk_i32 s28, 0x2000
	s_branch .Lxp_dcom0
.Lxp_wnp0:
	s_movk_i32 s26, 0x2000
	s_mov_b32 s27, 0x1a000
	s_mov_b32 s28, 0x8000
.Lxp_dcom0:
	s_movk_i32 s63, 0x800
	s_lshl_b32 s57, s65, 7
	s_mul_i32 s57, s57, s87
	s_add_u32 s56, s56, s57
	s_lshl_b32 s57, s67, 8
	s_add_u32 s56, s56, s57
	s_lshl_b32 s57, s67, 17
	s_add_u32 s57, s57, s86
	s_lshl_b32 s66, s65, 7
	s_add_u32 s57, s57, s66
.Lxp_tail0:
	s_add_u32 s24, s68, s56
	s_addc_u32 s25, s69, 0
	s_add_u32 s60, s8, s57
	s_addc_u32 s61, s9, 0
	s_lshl_b32 s62, s63, 3
	v_mov_b32_e32 v216, v175
	v_mov_b32_e32 v214, 0x42000000
	s_cmp_eq_u32 s81, 0
	s_cbranch_scc1 .Lxp_nopad0
	v_mov_b32_e32 v216, v218
	v_mov_b32_e32 v214, v217
.Lxp_nopad0:
	v_mov_b32_e32 v215, v214
	v_mad_u32_u24 v170, v174, s28, v216
	global_load_dwordx4 v[0:3], v170, s[24:25]
	s_add_u32 s24, s24, s26
	s_addc_u32 s25, s25, 0
	global_load_dwordx4 v[4:7], v170, s[24:25]
	s_add_u32 s24, s24, s26
	s_addc_u32 s25, s25, 0
	global_load_dwordx4 v[8:11], v170, s[24:25]
	s_add_u32 s24, s24, s26
	s_addc_u32 s25, s25, 0
	global_load_dwordx4 v[12:15], v170, s[24:25]
	s_add_u32 s24, s24, s27
	s_addc_u32 s25, s25, s80
	global_load_dwordx4 v[16:19], v170, s[24:25]
	s_add_u32 s24, s24, s26
	s_addc_u32 s25, s25, 0
	global_load_dwordx4 v[20:23], v170, s[24:25]
	s_add_u32 s24, s24, s26
	s_addc_u32 s25, s25, 0
	global_load_dwordx4 v[24:27], v170, s[24:25]
	s_add_u32 s24, s24, s26
	s_addc_u32 s25, s25, 0
	global_load_dwordx4 v[28:31], v170, s[24:25]
	s_add_u32 s24, s24, s27
	s_addc_u32 s25, s25, s80
	global_load_dwordx4 v[32:35], v170, s[24:25]
	s_add_u32 s24, s24, s26
	s_addc_u32 s25, s25, 0
	global_load_dwordx4 v[36:39], v170, s[24:25]
	s_add_u32 s24, s24, s26
	s_addc_u32 s25, s25, 0
	global_load_dwordx4 v[40:43], v170, s[24:25]
	s_add_u32 s24, s24, s26
	s_addc_u32 s25, s25, 0
	global_load_dwordx4 v[44:47], v170, s[24:25]
	s_add_u32 s24, s24, s27
	s_addc_u32 s25, s25, s80
	global_load_dwordx4 v[48:51], v170, s[24:25]
	s_add_u32 s24, s24, s26
	s_addc_u32 s25, s25, 0
	global_load_dwordx4 v[52:55], v170, s[24:25]
	s_add_u32 s24, s24, s26
	s_addc_u32 s25, s25, 0
	global_load_dwordx4 v[56:59], v170, s[24:25]
	s_add_u32 s24, s24, s26
	s_addc_u32 s25, s25, 0
	global_load_dwordx4 v[60:63], v170, s[24:25]
	s_add_u32 s24, s24, s27
	s_addc_u32 s25, s25, s80
	global_load_dwordx4 v[64:67], v170, s[24:25]
	s_add_u32 s24, s24, s26
	s_addc_u32 s25, s25, 0
	global_load_dwordx4 v[68:71], v170, s[24:25]
	s_add_u32 s24, s24, s26
	s_addc_u32 s25, s25, 0
	global_load_dwordx4 v[72:75], v170, s[24:25]
	s_add_u32 s24, s24, s26
	s_addc_u32 s25, s25, 0
	global_load_dwordx4 v[76:79], v170, s[24:25]
	s_add_u32 s24, s24, s27
	s_addc_u32 s25, s25, s80
	global_load_dwordx4 v[80:83], v170, s[24:25]
	s_add_u32 s24, s24, s26
	s_addc_u32 s25, s25, 0
	global_load_dwordx4 v[84:87], v170, s[24:25]
	s_add_u32 s24, s24, s26
	s_addc_u32 s25, s25, 0
	global_load_dwordx4 v[88:91], v170, s[24:25]
	s_add_u32 s24, s24, s26
	s_addc_u32 s25, s25, 0
	global_load_dwordx4 v[92:95], v170, s[24:25]
	s_add_u32 s24, s24, s27
	s_addc_u32 s25, s25, s80
	global_load_dwordx4 v[96:99], v170, s[24:25]
	s_add_u32 s24, s24, s26
	s_addc_u32 s25, s25, 0
	global_load_dwordx4 v[100:103], v170, s[24:25]
	s_add_u32 s24, s24, s26
	s_addc_u32 s25, s25, 0
	global_load_dwordx4 v[104:107], v170, s[24:25]
	s_add_u32 s24, s24, s26
	s_addc_u32 s25, s25, 0
	global_load_dwordx4 v[108:111], v170, s[24:25]
	s_add_u32 s24, s24, s27
	s_addc_u32 s25, s25, s80
	global_load_dwordx4 v[112:115], v170, s[24:25]
	s_add_u32 s24, s24, s26
	s_addc_u32 s25, s25, 0
	global_load_dwordx4 v[116:119], v170, s[24:25]
	s_add_u32 s24, s24, s26
	s_addc_u32 s25, s25, 0
	global_load_dwordx4 v[120:123], v170, s[24:25]
	s_add_u32 s24, s24, s26
	s_addc_u32 s25, s25, 0
	global_load_dwordx4 v[124:127], v170, s[24:25]
	s_add_u32 s24, s24, s27
	s_addc_u32 s25, s25, s80
	global_load_dwordx4 v[180:183], v175, s[2:3]
	global_load_dwordx4 v[184:187], v175, s[2:3]
	global_load_dwordx4 v[188:191], v175, s[2:3]
	global_load_dwordx4 v[192:195], v175, s[2:3]
	global_load_dwordx4 v[196:199], v175, s[2:3]
	global_load_dwordx4 v[200:203], v175, s[2:3]
	global_load_dwordx4 v[204:207], v175, s[2:3]
	global_load_dwordx4 v[208:211], v175, s[2:3]
.Lxc_loop:
	s_mov_b64 s[14:15], s[60:61]
	s_mov_b32 s16, s62
	s_mov_b32 s17, s63
	v_mov_b32_e32 v178, v214
	v_mov_b32_e32 v179, v215
	s_mov_b32 s12, s13
	s_add_u32 s13, s12, s11
	s_cmp_lt_u32 s13, 0xcf00
	s_cbranch_scc0 .Lxc_tail
	s_mov_b32 s81, 0
	s_mov_b32 s80, 0
	s_cmp_lt_u32 s13, 0xc000
	s_cbranch_scc0 .Lxp_other1
	s_lshr_b32 s56, s13, 13
	s_and_b32 s57, s13, 0x1fff
	s_mov_b32 s85, 0
	s_branch .Lxp_exp1

.Lxp_nopad1:
	v_mov_b32_e32 v215, v214
	v_mad_u32_u24 v170, v174, s28, v216
	s_waitcnt vmcnt(36)
	v_pk_mul_f32 v[0:1], v[0:1], v[178:179]
	v_pk_mul_f32 v[2:3], v[2:3], v[178:179]
	v_pk_mul_f32 v[4:5], v[4:5], v[178:179]
	v_pk_mul_f32 v[6:7], v[6:7], v[178:179]
	v_pk_mul_f32 v[8:9], v[8:9], v[178:179]
	v_pk_mul_f32 v[10:11], v[10:11], v[178:179]
	v_pk_mul_f32 v[12:13], v[12:13], v[178:179]
	v_pk_mul_f32 v[14:15], v[14:15], v[178:179]
	v_cvt_pk_fp8_f32 v128, v0, v4
	v_cvt_pk_fp8_f32 v129, v1, v5
	v_cvt_pk_fp8_f32 v130, v2, v6
	v_cvt_pk_fp8_f32 v131, v3, v7
	v_cvt_pk_fp8_f32 v128, v8, v12 op_sel:[0,0,1]
	v_cvt_pk_fp8_f32 v129, v9, v13 op_sel:[0,0,1]
	v_cvt_pk_fp8_f32 v130, v10, v14 op_sel:[0,0,1]
	v_cvt_pk_fp8_f32 v131, v11, v15 op_sel:[0,0,1]
	global_load_dwordx4 v[0:3], v170, s[24:25]
	s_add_u32 s24, s24, s26
	s_addc_u32 s25, s25, 0
	global_load_dwordx4 v[4:7], v170, s[24:25]
	s_add_u32 s24, s24, s26
	s_addc_u32 s25, s25, 0
	global_load_dwordx4 v[8:11], v170, s[24:25]
	s_add_u32 s24, s24, s26
	s_addc_u32 s25, s25, 0
	global_load_dwordx4 v[12:15], v170, s[24:25]
	s_add_u32 s24, s24, s27
	s_addc_u32 s25, s25, s80
	ds_write_b32 v172, v128 offset:0
	ds_write_b32 v172, v129 offset:132
	ds_write_b32 v172, v130 offset:264
	ds_write_b32 v172, v131 offset:396
	s_waitcnt vmcnt(36)
	v_pk_mul_f32 v[16:17], v[16:17], v[178:179]
	v_pk_mul_f32 v[18:19], v[18:19], v[178:179]
	v_pk_mul_f32 v[20:21], v[20:21], v[178:179]
	v_pk_mul_f32 v[22:23], v[22:23], v[178:179]
	v_pk_mul_f32 v[24:25], v[24:25], v[178:179]
	v_pk_mul_f32 v[26:27], v[26:27], v[178:179]
	v_pk_mul_f32 v[28:29], v[28:29], v[178:179]
	v_pk_mul_f32 v[30:31], v[30:31], v[178:179]
	v_cvt_pk_fp8_f32 v132, v16, v20
	v_cvt_pk_fp8_f32 v133, v17, v21
	v_cvt_pk_fp8_f32 v134, v18, v22
	v_cvt_pk_fp8_f32 v135, v19, v23
	v_cvt_pk_fp8_f32 v132, v24, v28 op_sel:[0,0,1]
	v_cvt_pk_fp8_f32 v133, v25, v29 op_sel:[0,0,1]
	v_cvt_pk_fp8_f32 v134, v26, v30 op_sel:[0,0,1]
	v_cvt_pk_fp8_f32 v135, v27, v31 op_sel:[0,0,1]
	global_load_dwordx4 v[16:19], v170, s[24:25]
	s_add_u32 s24, s24, s26
	s_addc_u32 s25, s25, 0
	global_load_dwordx4 v[20:23], v170, s[24:25]
	s_add_u32 s24, s24, s26
	s_addc_u32 s25, s25, 0
	global_load_dwordx4 v[24:27], v170, s[24:25]
	s_add_u32 s24, s24, s26
	s_addc_u32 s25, s25, 0
	global_load_dwordx4 v[28:31], v170, s[24:25]
	s_add_u32 s24, s24, s27
	s_addc_u32 s25, s25, s80
	ds_write_b32 v172, v132 offset:16
	ds_write_b32 v172, v133 offset:148
	ds_write_b32 v172, v134 offset:280
	ds_write_b32 v172, v135 offset:412
	s_waitcnt vmcnt(36)
	v_pk_mul_f32 v[32:33], v[32:33], v[178:179]
	v_pk_mul_f32 v[34:35], v[34:35], v[178:179]
	v_pk_mul_f32 v[36:37], v[36:37], v[178:179]
	v_pk_mul_f32 v[38:39], v[38:39], v[178:179]
	v_pk_mul_f32 v[40:41], v[40:41], v[178:179]
	v_pk_mul_f32 v[42:43], v[42:43], v[178:179]
	v_pk_mul_f32 v[44:45], v[44:45], v[178:179]
	v_pk_mul_f32 v[46:47], v[46:47], v[178:179]
	v_cvt_pk_fp8_f32 v128, v32, v36
	v_cvt_pk_fp8_f32 v129, v33, v37
	v_cvt_pk_fp8_f32 v130, v34, v38
	v_cvt_pk_fp8_f32 v131, v35, v39
	v_cvt_pk_fp8_f32 v128, v40, v44 op_sel:[0,0,1]
	v_cvt_pk_fp8_f32 v129, v41, v45 op_sel:[0,0,1]
	v_cvt_pk_fp8_f32 v130, v42, v46 op_sel:[0,0,1]
	v_cvt_pk_fp8_f32 v131, v43, v47 op_sel:[0,0,1]
	global_load_dwordx4 v[32:35], v170, s[24:25]
	s_add_u32 s24, s24, s26
	s_addc_u32 s25, s25, 0
	global_load_dwordx4 v[36:39], v170, s[24:25]
	s_add_u32 s24, s24, s26
	s_addc_u32 s25, s25, 0
	global_load_dwordx4 v[40:43], v170, s[24:25]
	s_add_u32 s24, s24, s26
	s_addc_u32 s25, s25, 0
	global_load_dwordx4 v[44:47], v170, s[24:25]
	s_add_u32 s24, s24, s27
	s_addc_u32 s25, s25, s80
	ds_write_b32 v172, v128 offset:32
	ds_write_b32 v172, v129 offset:164
	ds_write_b32 v172, v130 offset:296
	ds_write_b32 v172, v131 offset:428
	s_waitcnt vmcnt(36)
	v_pk_mul_f32 v[48:49], v[48:49], v[178:179]
	v_pk_mul_f32 v[50:51], v[50:51], v[178:179]
	v_pk_mul_f32 v[52:53], v[52:53], v[178:179]
	v_pk_mul_f32 v[54:55], v[54:55], v[178:179]
	v_pk_mul_f32 v[56:57], v[56:57], v[178:179]
	v_pk_mul_f32 v[58:59], v[58:59], v[178:179]
	v_pk_mul_f32 v[60:61], v[60:61], v[178:179]
	v_pk_mul_f32 v[62:63], v[62:63], v[178:179]
	v_cvt_pk_fp8_f32 v132, v48, v52
	v_cvt_pk_fp8_f32 v133, v49, v53
	v_cvt_pk_fp8_f32 v134, v50, v54
	v_cvt_pk_fp8_f32 v135, v51, v55
	v_cvt_pk_fp8_f32 v132, v56, v60 op_sel:[0,0,1]
	v_cvt_pk_fp8_f32 v133, v57, v61 op_sel:[0,0,1]
	v_cvt_pk_fp8_f32 v134, v58, v62 op_sel:[0,0,1]
	v_cvt_pk_fp8_f32 v135, v59, v63 op_sel:[0,0,1]
	global_load_dwordx4 v[48:51], v170, s[24:25]
	s_add_u32 s24, s24, s26
	s_addc_u32 s25, s25, 0
	global_load_dwordx4 v[52:55], v170, s[24:25]
	s_add_u32 s24, s24, s26
	s_addc_u32 s25, s25, 0
	global_load_dwordx4 v[56:59], v170, s[24:25]
	s_add_u32 s24, s24, s26
	s_addc_u32 s25, s25, 0
	global_load_dwordx4 v[60:63], v170, s[24:25]
	s_add_u32 s24, s24, s27
	s_addc_u32 s25, s25, s80
	ds_write_b32 v172, v132 offset:48
	ds_write_b32 v172, v133 offset:180
	ds_write_b32 v172, v134 offset:312
	ds_write_b32 v172, v135 offset:444
	s_waitcnt vmcnt(36)
	v_pk_mul_f32 v[64:65], v[64:65], v[178:179]
	v_pk_mul_f32 v[66:67], v[66:67], v[178:179]
	v_pk_mul_f32 v[68:69], v[68:69], v[178:179]
	v_pk_mul_f32 v[70:71], v[70:71], v[178:179]
	v_pk_mul_f32 v[72:73], v[72:73], v[178:179]
	v_pk_mul_f32 v[74:75], v[74:75], v[178:179]
	v_pk_mul_f32 v[76:77], v[76:77], v[178:179]
	v_pk_mul_f32 v[78:79], v[78:79], v[178:179]
	v_cvt_pk_fp8_f32 v128, v64, v68
	v_cvt_pk_fp8_f32 v129, v65, v69
	v_cvt_pk_fp8_f32 v130, v66, v70
	v_cvt_pk_fp8_f32 v131, v67, v71
	v_cvt_pk_fp8_f32 v128, v72, v76 op_sel:[0,0,1]
	v_cvt_pk_fp8_f32 v129, v73, v77 op_sel:[0,0,1]
	v_cvt_pk_fp8_f32 v130, v74, v78 op_sel:[0,0,1]
	v_cvt_pk_fp8_f32 v131, v75, v79 op_sel:[0,0,1]
	global_load_dwordx4 v[64:67], v170, s[24:25]
	s_add_u32 s24, s24, s26
	s_addc_u32 s25, s25, 0
	global_load_dwordx4 v[68:71], v170, s[24:25]
	s_add_u32 s24, s24, s26
	s_addc_u32 s25, s25, 0
	global_load_dwordx4 v[72:75], v170, s[24:25]
	s_add_u32 s24, s24, s26
	s_addc_u32 s25, s25, 0
	global_load_dwordx4 v[76:79], v170, s[24:25]
	s_add_u32 s24, s24, s27
	s_addc_u32 s25, s25, s80
	ds_write_b32 v172, v128 offset:64
	ds_write_b32 v172, v129 offset:196
	ds_write_b32 v172, v130 offset:328
	ds_write_b32 v172, v131 offset:460
	s_waitcnt vmcnt(36)
	v_pk_mul_f32 v[80:81], v[80:81], v[178:179]
	v_pk_mul_f32 v[82:83], v[82:83], v[178:179]
	v_pk_mul_f32 v[84:85], v[84:85], v[178:179]
	v_pk_mul_f32 v[86:87], v[86:87], v[178:179]
	v_pk_mul_f32 v[88:89], v[88:89], v[178:179]
	v_pk_mul_f32 v[90:91], v[90:91], v[178:179]
	v_pk_mul_f32 v[92:93], v[92:93], v[178:179]
	v_pk_mul_f32 v[94:95], v[94:95], v[178:179]
	v_cvt_pk_fp8_f32 v132, v80, v84
	v_cvt_pk_fp8_f32 v133, v81, v85
	v_cvt_pk_fp8_f32 v134, v82, v86
	v_cvt_pk_fp8_f32 v135, v83, v87
	v_cvt_pk_fp8_f32 v132, v88, v92 op_sel:[0,0,1]
	v_cvt_pk_fp8_f32 v133, v89, v93 op_sel:[0,0,1]
	v_cvt_pk_fp8_f32 v134, v90, v94 op_sel:[0,0,1]
	v_cvt_pk_fp8_f32 v135, v91, v95 op_sel:[0,0,1]
	global_load_dwordx4 v[80:83], v170, s[24:25]
	s_add_u32 s24, s24, s26
	s_addc_u32 s25, s25, 0
	global_load_dwordx4 v[84:87], v170, s[24:25]
	s_add_u32 s24, s24, s26
	s_addc_u32 s25, s25, 0
	global_load_dwordx4 v[88:91], v170, s[24:25]
	s_add_u32 s24, s24, s26
	s_addc_u32 s25, s25, 0
	global_load_dwordx4 v[92:95], v170, s[24:25]
	s_add_u32 s24, s24, s27
	s_addc_u32 s25, s25, s80
	ds_write_b32 v172, v132 offset:80
	ds_write_b32 v172, v133 offset:212
	ds_write_b32 v172, v134 offset:344
	ds_write_b32 v172, v135 offset:476
	s_waitcnt vmcnt(36)
	v_pk_mul_f32 v[96:97], v[96:97], v[178:179]
	v_pk_mul_f32 v[98:99], v[98:99], v[178:179]
	v_pk_mul_f32 v[100:101], v[100:101], v[178:179]
	v_pk_mul_f32 v[102:103], v[102:103], v[178:179]
	v_pk_mul_f32 v[104:105], v[104:105], v[178:179]
	v_pk_mul_f32 v[106:107], v[106:107], v[178:179]
	v_pk_mul_f32 v[108:109], v[108:109], v[178:179]
	v_pk_mul_f32 v[110:111], v[110:111], v[178:179]
	v_cvt_pk_fp8_f32 v128, v96, v100
	v_cvt_pk_fp8_f32 v129, v97, v101
	v_cvt_pk_fp8_f32 v130, v98, v102
	v_cvt_pk_fp8_f32 v131, v99, v103
	v_cvt_pk_fp8_f32 v128, v104, v108 op_sel:[0,0,1]
	v_cvt_pk_fp8_f32 v129, v105, v109 op_sel:[0,0,1]
	v_cvt_pk_fp8_f32 v130, v106, v110 op_sel:[0,0,1]
	v_cvt_pk_fp8_f32 v131, v107, v111 op_sel:[0,0,1]
	global_load_dwordx4 v[96:99], v170, s[24:25]
	s_add_u32 s24, s24, s26
	s_addc_u32 s25, s25, 0
	global_load_dwordx4 v[100:103], v170, s[24:25]
	s_add_u32 s24, s24, s26
	s_addc_u32 s25, s25, 0
	global_load_dwordx4 v[104:107], v170, s[24:25]
	s_add_u32 s24, s24, s26
	s_addc_u32 s25, s25, 0
	global_load_dwordx4 v[108:111], v170, s[24:25]
	s_add_u32 s24, s24, s27
	s_addc_u32 s25, s25, s80
	ds_write_b32 v172, v128 offset:96
	ds_write_b32 v172, v129 offset:228
	ds_write_b32 v172, v130 offset:360
	ds_write_b32 v172, v131 offset:492
	s_waitcnt vmcnt(36)
	v_pk_mul_f32 v[112:113], v[112:113], v[178:179]
	v_pk_mul_f32 v[114:115], v[114:115], v[178:179]
	v_pk_mul_f32 v[116:117], v[116:117], v[178:179]
	v_pk_mul_f32 v[118:119], v[118:119], v[178:179]
	v_pk_mul_f32 v[120:121], v[120:121], v[178:179]
	v_pk_mul_f32 v[122:123], v[122:123], v[178:179]
	v_pk_mul_f32 v[124:125], v[124:125], v[178:179]
	v_pk_mul_f32 v[126:127], v[126:127], v[178:179]
	v_cvt_pk_fp8_f32 v132, v112, v116
	v_cvt_pk_fp8_f32 v133, v113, v117
	v_cvt_pk_fp8_f32 v134, v114, v118
	v_cvt_pk_fp8_f32 v135, v115, v119
	v_cvt_pk_fp8_f32 v132, v120, v124 op_sel:[0,0,1]
	v_cvt_pk_fp8_f32 v133, v121, v125 op_sel:[0,0,1]
	v_cvt_pk_fp8_f32 v134, v122, v126 op_sel:[0,0,1]
	v_cvt_pk_fp8_f32 v135, v123, v127 op_sel:[0,0,1]
	global_load_dwordx4 v[112:115], v170, s[24:25]
	s_add_u32 s24, s24, s26
	s_addc_u32 s25, s25, 0
	global_load_dwordx4 v[116:119], v170, s[24:25]
	s_add_u32 s24, s24, s26
	s_addc_u32 s25, s25, 0
	global_load_dwordx4 v[120:123], v170, s[24:25]
	s_add_u32 s24, s24, s26
	s_addc_u32 s25, s25, 0
	global_load_dwordx4 v[124:127], v170, s[24:25]
	s_add_u32 s24, s24, s27
	s_addc_u32 s25, s25, s80
	ds_write_b32 v172, v132 offset:112
	ds_write_b32 v172, v133 offset:244
	ds_write_b32 v172, v134 offset:376
	ds_write_b32 v172, v135 offset:508
	v_mad_u32_u24 v171, v176, s17, v177
	ds_read_b32 v136, v173 offset:0
	ds_read_b32 v137, v173 offset:4
	ds_read_b32 v138, v173 offset:8
	ds_read_b32 v139, v173 offset:12
	ds_read_b32 v140, v173 offset:1056
	ds_read_b32 v141, v173 offset:1060
	ds_read_b32 v142, v173 offset:1064
	ds_read_b32 v143, v173 offset:1068
	ds_read_b32 v144, v173 offset:2112
	ds_read_b32 v145, v173 offset:2116
	ds_read_b32 v146, v173 offset:2120
	ds_read_b32 v147, v173 offset:2124
	ds_read_b32 v148, v173 offset:3168
	ds_read_b32 v149, v173 offset:3172
	ds_read_b32 v150, v173 offset:3176
	ds_read_b32 v151, v173 offset:3180
	s_waitcnt lgkmcnt(12)
	global_store_dwordx4 v171, v[136:139], s[14:15]
	s_add_u32 s14, s14, s16
	s_addc_u32 s15, s15, 0
	s_waitcnt lgkmcnt(8)
	global_store_dwordx4 v171, v[140:143], s[14:15]
	s_add_u32 s14, s14, s16
	s_addc_u32 s15, s15, 0
	s_waitcnt lgkmcnt(4)
	global_store_dwordx4 v171, v[144:147], s[14:15]
	s_add_u32 s14, s14, s16
	s_addc_u32 s15, s15, 0
	s_waitcnt lgkmcnt(0)
	global_store_dwordx4 v171, v[148:151], s[14:15]
	s_add_u32 s14, s14, s16
	s_addc_u32 s15, s15, 0
	ds_read_b32 v152, v173 offset:4224
	ds_read_b32 v153, v173 offset:4228
	ds_read_b32 v154, v173 offset:4232
	ds_read_b32 v155, v173 offset:4236
	ds_read_b32 v156, v173 offset:5280
	ds_read_b32 v157, v173 offset:5284
	ds_read_b32 v158, v173 offset:5288
	ds_read_b32 v159, v173 offset:5292
	ds_read_b32 v160, v173 offset:6336
	ds_read_b32 v161, v173 offset:6340
	ds_read_b32 v162, v173 offset:6344
	ds_read_b32 v163, v173 offset:6348
	ds_read_b32 v164, v173 offset:7392
	ds_read_b32 v165, v173 offset:7396
	ds_read_b32 v166, v173 offset:7400
	ds_read_b32 v167, v173 offset:7404
	s_waitcnt lgkmcnt(12)
	global_store_dwordx4 v171, v[152:155], s[14:15]
	s_add_u32 s14, s14, s16
	s_addc_u32 s15, s15, 0
	s_waitcnt lgkmcnt(8)
	global_store_dwordx4 v171, v[156:159], s[14:15]
	s_add_u32 s14, s14, s16
	s_addc_u32 s15, s15, 0
	s_waitcnt lgkmcnt(4)
	global_store_dwordx4 v171, v[160:163], s[14:15]
	s_add_u32 s14, s14, s16
	s_addc_u32 s15, s15, 0
	s_waitcnt lgkmcnt(0)
	global_store_dwordx4 v171, v[164:167], s[14:15]
	s_add_u32 s14, s14, s16
	s_addc_u32 s15, s15, 0
	s_branch .Lxc_loop
